# same as previous (router+nops+logf+hg_a) plus 12 bytes of unreachable padding so that later code keeps its 64-byte phase
# baseline (speedup 1.0000x reference)
; template <bool WITHO, bool RAW = false>
; __device__ __forceinline__ void hg_pass(const Frame& F, const bf16_t* P, const float* lbh, int b, int h, int nb, int dir, f32x4 (&S)[4][4], float (&Gsum)[16],
;                                         LAS bf16_t* Vl, LAS bf16_t* Kl, float* OF, const float* ngp) {
;     ...
;             if (dir == 0 || RAW) {
; #pragma unroll
;                 for (int i = 0; i < 4; ++i)
; #pragma unroll
;                     for (int vt = 0; vt < 4; ++vt) OF[(size_t)orow[i] * 512 + h * 64 + 16 * vt + tau] = o[vt][i];
.LBB0_1176:
	s_andn2_b64 vcc, exec, s[6:7]
	s_cbranch_vccnz .LBB0_1169
	v_lshlrev_b64 v[172:173], 11, v[172:173]
	v_lshlrev_b64 v[90:91], 11, v[90:91]
	v_lshlrev_b64 v[86:87], 11, v[86:87]
	v_lshlrev_b64 v[70:71], 11, v[70:71]
	v_lshl_add_u64 v[172:173], v[130:131], 0, v[172:173]
	v_lshl_add_u64 v[90:91], v[130:131], 0, v[90:91]
	v_lshl_add_u64 v[86:87], v[130:131], 0, v[86:87]
	v_lshl_add_u64 v[70:71], v[130:131], 0, v[70:71]
	global_store_dword v[172:173], v94, off
	global_store_dword v[172:173], v98, off offset:64
	global_store_dword v[172:173], v102, off offset:128
	global_store_dword v[172:173], v106, off offset:192
	global_store_dword v[90:91], v95, off
	global_store_dword v[90:91], v99, off offset:64
	global_store_dword v[90:91], v103, off offset:128
	global_store_dword v[90:91], v107, off offset:192
	global_store_dword v[86:87], v96, off
	global_store_dword v[86:87], v100, off offset:64
	global_store_dword v[86:87], v104, off offset:128
	global_store_dword v[86:87], v108, off offset:192
	global_store_dword v[70:71], v97, off
	global_store_dword v[70:71], v101, off offset:64
	global_store_dword v[70:71], v105, off offset:128
	global_store_dword v[70:71], v109, off offset:192
	s_branch .LBB0_1169
	s_nop 0
	s_nop 0
	s_nop 0
